# MoBA tile loop: six K/V slots, tile t+4 requested at step t, one barrier per two steps
# speedup vs baseline: 1.0041x; 1.0022x over previous
; #define ATT_WAIT_BAR(N) asm volatile("s_waitcnt vmcnt(" #N ") lgkmcnt(0)\n\ts_barrier" ::: "memory")
; #define ATT_DMA(t, slot) do { glds16(ksrc + (long)(t) * tstep, (unsigned)__builtin_amdgcn_readfirstlane(kdst + (slot))); glds16(vsrc + (long)(t) * tstep, (unsigned)__builtin_amdgcn_readfirstlane(vdst + (slot))); } while (0)
; template <class BIAS>
; __device__ __forceinline__ void attn_tiles(char* shm, const UnitIO& io, int t_begin, int t_end, const BIAS& B, int tid) {
;     ...
;     bf16x8 qr[4];
;     { const bf16* qp = io.Q + (long)r32 * io.qstride + hi * 8;
; #pragma unroll
;       for (int d0 = 0; d0 < 4; ++d0) qr[d0] = *reinterpret_cast<const bf16x8*>(qp + d0 * 16); }
;     ATT_DMA(t_begin, 0);
;     asm volatile("" :: "v"(qr[0]), "v"(qr[1]), "v"(qr[2]), "v"(qr[3]));
;     const int nt_ = t_end - t_begin; if (nt_ > 1) ATT_DMA(t_begin + 1, SLOTB); if (nt_ > 2) ATT_DMA(t_begin + 2, 2 * SLOTB);
;     f32x16 o[2]; o[0] = f32x16{}; o[1] = f32x16{}; float l_reg = 0.f;
;     if (nt_ > 2) ATT_WAIT_BAR(4); else if (nt_ > 1) ATT_WAIT_BAR(2); else ATT_WAIT_BAR(0);
.LBB0_294:
	v_lshlrev_b32_e64 v2, v41, 1
	v_cmp_lt_i32_e32 vcc, -1, v41
	v_lshlrev_b32_e64 v3, v5, 1
	v_lshlrev_b32_e32 v148, 1, v154
	v_cndmask_b32_e32 v2, 0, v2, vcc
	v_cmp_lt_i32_e32 vcc, -1, v5
	v_lshlrev_b32_e64 v5, v4, 1
	v_mov_b32_e32 v149, v1
	v_cndmask_b32_e32 v3, 0, v3, vcc
	v_cmp_lt_i32_e32 vcc, -1, v4
	v_readfirstlane_b32 s27, v232
	s_ashr_i32 s16, s27, 6
	v_cndmask_b32_e32 v4, 0, v5, vcc
	v_or3_b32 v135, v3, v2, v4
	v_add_u32_e32 v2, s22, v143
	v_cvt_f32_i32_e32 v137, v2
	v_lshl_add_u64 v[2:3], s[4:5], 0, v[132:133]
	v_lshl_add_u64 v[2:3], v[2:3], 0, v[148:149]
	flat_load_dwordx4 v[66:69], v[2:3]
	flat_load_dwordx4 v[70:73], v[2:3] offset:32
	flat_load_dwordx4 v[74:77], v[2:3] offset:64
	flat_load_dwordx4 v[78:81], v[2:3] offset:96
	s_lshl_b32 s12, s16, 4
	v_and_or_b32 v4, s12, 48, v178
	s_ashr_i32 s12, s27, 3
	s_lshl_b32 s14, s16, 3
	s_andn2_b32 s12, s12, 31
	s_ashr_i32 s15, s14, 31
	s_ashr_i32 s13, s12, 31
	v_lshlrev_b32_e32 v4, 11, v4
	v_mov_b32_e32 v5, v1
	s_lshl_b64 s[4:5], s[14:15], 1
	v_lshl_add_u64 v[4:5], s[30:31], 0, v[4:5]
	s_lshl_b64 s[12:13], s[12:13], 1
	s_lshl_b32 s29, s16, 10
	v_lshl_add_u64 v[2:3], v[156:157], 0, s[4:5]
	v_lshl_add_u64 v[2:3], v[2:3], 0, v[244:245]
	v_lshl_add_u64 v[4:5], v[4:5], 0, s[12:13]
	v_lshlrev_b32_e32 v150, 1, v144
	v_mov_b32_e32 v151, v1
	s_mov_b32 s14, m0
	s_mov_b32 m0, s29
	s_nop 0
	global_load_lds_dwordx4 v[2:3], off
	s_mov_b32 m0, s14
	s_add_i32 s33, s29, 0x8000
	v_lshl_add_u64 v[4:5], v[4:5], 0, v[150:151]
	s_mov_b32 s14, m0
	s_mov_b32 m0, s33
	s_nop 0
	global_load_lds_dwordx4 v[4:5], off
	s_mov_b32 m0, s14
	s_mov_b64 s[22:23], 0x20000
	s_add_i32 s14, s29, 0x2000
	v_lshl_add_u64 v[6:7], v[2:3], 0, s[22:23]
	v_mov_b32_e32 v16, v1
	v_mov_b32_e32 v17, v1
	s_lshl_b32 s26, s20, 2
	v_mov_b32_e32 v8, v1
	v_mov_b32_e32 v9, v1
	v_mov_b32_e32 v10, v1
	v_mov_b32_e32 v11, v1
	v_mov_b32_e32 v12, v1
	v_mov_b32_e32 v13, v1
	v_mov_b32_e32 v14, v1
	v_mov_b32_e32 v15, v1
	s_lshl_b64 s[10:11], s[10:11], 10
	s_mov_b32 s17, 0
	s_add_i32 s28, s26, 4
	v_lshl_add_u64 v[172:173], v[166:167], 0, s[4:5]
	v_lshl_add_u64 v[172:173], v[172:173], 0, v[244:245]
	s_sub_i32 s20, 0, s26
	s_sub_i32 s24, s72, s26
	v_mov_b32_e32 v139, 0
	v_mov_b32_e32 v149, v145
	s_waitcnt vmcnt(0) lgkmcnt(0)
	s_mov_b32 s15, m0
	s_mov_b32 m0, s14
	s_nop 0
	global_load_lds_dwordx4 v[6:7], off
	s_mov_b32 m0, s15
	s_add_i32 s14, s33, 0x2000
	v_lshl_add_u64 v[6:7], v[4:5], 0, s[22:23]
	s_mov_b32 s15, m0
	s_mov_b32 m0, s14
	s_nop 0
	global_load_lds_dwordx4 v[6:7], off
	s_mov_b32 m0, s15
	s_mov_b64 s[22:23], 0x40000
	s_add_i32 s14, s29, 0x4000
	v_lshl_add_u64 v[2:3], v[2:3], 0, s[22:23]
	s_mov_b32 s15, m0
	s_mov_b32 m0, s14
	s_nop 0
	global_load_lds_dwordx4 v[2:3], off
	s_mov_b32 m0, s15
	s_add_i32 s14, s33, 0x4000
	v_lshl_add_u64 v[2:3], v[4:5], 0, s[22:23]
	s_mov_b32 s15, m0
	s_mov_b32 m0, s14
	s_nop 0
	global_load_lds_dwordx4 v[2:3], off
	s_mov_b32 m0, s15
	s_lshl_b32 s14, s16, 15
	s_and_b32 s14, s14, 0x18000
	v_lshl_or_b32 v2, v175, 1, s14
	v_mov_b32_e32 v3, v1
	s_waitcnt vmcnt(2) lgkmcnt(0)
	s_barrier
	v_lshl_add_u64 v[2:3], s[12:13], 0, v[2:3]
	v_lshl_add_u64 v[152:153], v[164:165], 0, v[2:3]
	s_add_i32 s14, s29, 0x6000
	s_mov_b32 m0, s14
	s_add_i32 s14, s33, 0x6000
	global_load_lds_dwordx4 v[172:173], off
	s_mov_b32 m0, s14
	s_nop 0
	global_load_lds_dwordx4 v[152:153], off
	s_mov_b64 s[14:15], 0x20000
	v_lshl_add_u64 v[172:173], v[172:173], 0, s[14:15]
	v_lshl_add_u64 v[152:153], v[152:153], 0, s[14:15]
	v_mov_b32_e32 v2, v1
	v_mov_b32_e32 v3, v1
	v_mov_b32_e32 v4, v1
	v_mov_b32_e32 v5, v1
	v_mov_b32_e32 v6, v1
	v_mov_b32_e32 v7, v1
	v_mov_b64_e32 v[32:33], v[16:17]
	s_mov_b32 s22, 0
	v_mov_b64_e32 v[30:31], v[14:15]
	v_mov_b64_e32 v[28:29], v[12:13]
	v_mov_b64_e32 v[26:27], v[10:11]
	v_mov_b64_e32 v[24:25], v[8:9]
	v_mov_b64_e32 v[22:23], v[6:7]
	v_mov_b64_e32 v[20:21], v[4:5]
	v_mov_b64_e32 v[18:19], v[2:3]
	s_branch .LBB0_296
.LBB0_295:
	s_add_i32 s17, s17, 1
	s_mov_b64 s[4:5], 0x20000
	s_add_i32 s22, s22, 1
	s_cmp_eq_u32 s22, 6
	s_cselect_b32 s22, 0, s22
	v_lshl_add_u64 v[152:153], v[152:153], 0, s[4:5]
	v_lshl_add_u64 v[172:173], v[172:173], 0, s[4:5]
	s_add_i32 s4, s20, s17
	s_add_i32 s28, s28, -1
	s_cmp_eq_u32 s4, 4
	v_add_u32_e32 v149, 64, v149
	s_cbranch_scc1 .LBB0_314
.LBB0_296:
	s_cmp_lt_u32 s28, 5
	s_cselect_b64 s[12:13], -1, 0
; #define ATT_SBAR() __builtin_amdgcn_sched_barrier(0)
; #define ATT_DMA(t, slot) do { glds16(ksrc + (long)(t) * tstep, (unsigned)__builtin_amdgcn_readfirstlane(kdst + (slot))); glds16(vsrc + (long)(t) * tstep, (unsigned)__builtin_amdgcn_readfirstlane(vdst + (slot))); } while (0)
;     __device__ __forceinline__ void init(f32x16& c0, f32x16& c1, int t) const {
;         float base = slope2 * ((float)(64 * t + 4 * hi) - tqf);
;         if (t < nb0) { if (!((selmask >> (t >> 2)) & 1u)) base = ATT_NEG; }
;         const float d32 = 32.0f * slope2;
; #pragma unroll
;         for (int i = 0; i < 8; ++i) { const int r = 2 * i; const f32x2_t kc = (f32x2_t){slope2 * (float)((r & 3) + 8 * (r >> 2)), slope2 * (float)(((r + 1) & 3) + 8 * ((r + 1) >> 2))};
;             const f32x2_t p = kc + base, q = p + d32; c0[r] = p[0]; c0[r + 1] = p[1]; c1[r] = q[0]; c1[r + 1] = q[1]; }
; template <class BIAS>
; __device__ __forceinline__ void attn_tiles(char* shm, const UnitIO& io, int t_begin, int t_end, const BIAS& B, int tid) {
;     ...
;     for (int t = t_begin; t < t_end; ++t) {
;         const int rem = t_end - t;
;         const bool act = B.active(t);
;         const int sl_c = ((t - t_begin) & 3) * SLOTB;
;         if (rem > 3) ATT_DMA(t + 3, ((t + 3 - t_begin) & 3) * SLOTB);
;         u32x4 pw[4]; f32x16 c1x;
;         if (act) {
;             bf16x8 kf[8]; const lds_cptr kp = kp0 + sl_c;
; #pragma unroll
;             for (int j = 0; j < 4; ++j) { kf[2 * j] = *(const __attribute__((address_space(3))) bf16x8*)(kp + j * 2048); kf[2 * j + 1] = *(const __attribute__((address_space(3))) bf16x8*)(kp + j * 2048 + 512); }
;             ATT_SBAR();
;             f32x16 c0, c1; B.init(c0, c1, t);
;             ATT_SBAR();
;             asm volatile("" : "+v"(kf[0]), "+v"(kf[1]), "+v"(kf[2]), "+v"(kf[3]), "+v"(kf[4]), "+v"(kf[5]), "+v"(kf[6]), "+v"(kf[7]));
; #pragma unroll
;             for (int d0 = 0; d0 < 4; ++d0) { c0 = __builtin_amdgcn_mfma_f32_32x32x16_bf16(kf[2 * d0], qr[d0], c0, 0, 0, 0); c1 = __builtin_amdgcn_mfma_f32_32x32x16_bf16(kf[2 * d0 + 1], qr[d0], c1, 0, 0, 0); }
.LBB0_298:
	s_lshl_b32 s23, s22, 13
	s_cmp_gt_u32 s22, 3
	s_cselect_b32 s4, 0x14000, 0
	s_add_i32 s23, s23, s4
	s_add_i32 s34, s20, s17
	s_cmp_lt_u32 s17, s26
	s_cselect_b64 s[14:15], -1, 0
	s_cmp_le_i32 s34, s73
	s_cselect_b64 s[4:5], -1, 0
	s_or_b64 vcc, s[14:15], s[4:5]
	v_cndmask_b32_e64 v58, 0, 1, vcc
	v_cmp_ne_u32_e64 s[4:5], 1, v58
	s_andn2_b64 vcc, exec, vcc
	s_cbranch_vccnz .Lmo_inact
	v_add_u32_e32 v34, s23, v240
	v_add_u32_e32 v35, s23, v241
	v_add_u32_e32 v36, s23, v242
	v_add_u32_e32 v37, s23, v243
	ds_read_b128 v[98:101], v34
	ds_read_b128 v[94:97], v34 offset:4096
	ds_read_b128 v[102:105], v35
	ds_read_b128 v[90:93], v35 offset:4096
	ds_read_b128 v[106:109], v36
	ds_read_b128 v[86:89], v36 offset:4096
	ds_read_b128 v[110:113], v37
	ds_read_b128 v[82:85], v37 offset:4096
	s_add_i32 s35, s24, s17
	v_cvt_f32_u32_e32 v34, v149
	s_lshr_b32 vcc_lo, s17, 2
	s_lshl_b32 vcc_lo, 1, vcc_lo
	v_and_b32_e32 v35, vcc_lo, v135
	v_sub_f32_e32 v34, v34, v137
	v_cmp_eq_u32_e32 vcc, 0, v35
	v_mul_f32_e32 v34, v115, v34
	s_and_b64 vcc, s[14:15], vcc
	v_cndmask_b32_e32 v34, v34, v226, vcc
	v_add_f32_e32 v50, v114, v34
	v_add_f32_e32 v51, v115, v34
	v_add_f32_e32 v52, v118, v34
	v_add_f32_e32 v53, v119, v34
	v_add_f32_e32 v54, v120, v34
	v_add_f32_e32 v55, v121, v34
	v_add_f32_e32 v56, v122, v34
	v_add_f32_e32 v57, v123, v34
	v_add_f32_e32 v58, v124, v34
	v_add_f32_e32 v59, v125, v34
	v_add_f32_e32 v60, v126, v34
	v_add_f32_e32 v61, v127, v34
	v_add_f32_e32 v62, v128, v34
	v_add_f32_e32 v63, v129, v34
	v_add_f32_e32 v64, v140, v34
	v_add_f32_e32 v65, v141, v34
	v_mov_b32_e32 v117, v116
	v_add_f32_e32 v48, v116, v64
	v_add_f32_e32 v49, v117, v65
	v_add_f32_e32 v46, v116, v62
	v_add_f32_e32 v47, v117, v63
	v_add_f32_e32 v44, v116, v60
	v_add_f32_e32 v45, v117, v61
	v_add_f32_e32 v42, v116, v58
	v_add_f32_e32 v43, v117, v59
	v_add_f32_e32 v40, v116, v56
	v_add_f32_e32 v41, v117, v57
	v_add_f32_e32 v38, v116, v54
	v_add_f32_e32 v39, v117, v55
	v_add_f32_e32 v36, v116, v52
	v_add_f32_e32 v37, v117, v53
	s_cmp_lg_u32 s35, 0
	v_add_f32_e32 v34, v162, v50
	v_add_f32_e32 v35, v163, v51
	s_cbranch_scc1 .LBB0_303
	v_cndmask_b32_e64 v48, v48, v226, s[36:37]
	v_cndmask_b32_e64 v47, v47, v226, s[40:41]
	v_cndmask_b32_e64 v46, v46, v226, s[42:43]
	v_cndmask_b32_e64 v45, v45, v226, s[44:45]
	v_cndmask_b32_e64 v44, v44, v226, s[46:47]
	v_cndmask_b32_e64 v43, v43, v226, s[48:49]
	v_cndmask_b32_e64 v42, v42, v226, s[50:51]
	v_cndmask_b32_e64 v41, v41, v226, s[52:53]
	v_cndmask_b32_e64 v40, v40, v226, s[54:55]
	v_cndmask_b32_e64 v39, v39, v226, s[56:57]
	v_cndmask_b32_e64 v38, v38, v226, s[58:59]
	v_cndmask_b32_e64 v37, v37, v226, s[60:61]
	v_cndmask_b32_e64 v36, v36, v226, s[62:63]
	v_cndmask_b32_e64 v35, v35, v226, s[64:65]
	v_cndmask_b32_e64 v34, v34, v226, s[66:67]
	s_and_saveexec_b64 s[14:15], s[6:7]
	s_mov_b32 s35, 0xff800000
	v_mov_b32_e32 v49, s35
	s_or_b64 exec, exec, s[14:15]
	v_cndmask_b32_e64 v65, v65, v226, s[38:39]
	v_cndmask_b32_e64 v50, v50, v226, s[96:97]
	v_cndmask_b32_e64 v51, v51, v226, s[94:95]
	v_cndmask_b32_e64 v52, v52, v226, s[92:93]
	v_cndmask_b32_e64 v53, v53, v226, s[90:91]
	v_cndmask_b32_e64 v54, v54, v226, s[88:89]
	v_cndmask_b32_e64 v55, v55, v226, s[2:3]
	v_cndmask_b32_e64 v56, v56, v226, s[84:85]
	v_cndmask_b32_e64 v57, v57, v226, s[82:83]
	v_cndmask_b32_e64 v58, v58, v226, s[80:81]
	v_cndmask_b32_e64 v59, v59, v226, s[78:79]
	v_cndmask_b32_e64 v60, v60, v226, s[76:77]
	v_cndmask_b32_e64 v61, v61, v226, s[74:75]
	v_cndmask_b32_e64 v62, v62, v226, s[18:19]
	v_cndmask_b32_e64 v63, v63, v226, s[70:71]
	v_cndmask_b32_e64 v64, v64, v226, s[68:69]
.LBB0_303:
	s_waitcnt lgkmcnt(0)
	s_nop 0
	v_mfma_f32_32x32x16_bf16 v[50:65], v[98:101], v[66:69], v[50:65]
	v_mfma_f32_32x32x16_bf16 v[50:65], v[102:105], v[70:73], v[50:65]
	v_mfma_f32_32x32x16_bf16 v[50:65], v[106:109], v[74:77], v[50:65]
	v_mfma_f32_32x32x16_bf16 v[50:65], v[110:113], v[78:81], v[50:65]
	v_mfma_f32_32x32x16_bf16 v[34:49], v[94:97], v[66:69], v[34:49]
	s_and_b64 vcc, exec, s[12:13]
	s_cbranch_vccnz .Lmo_nodmaA
	s_add_i32 s100, s22, 4
	s_cmp_gt_u32 s100, 5
	s_cselect_b32 s101, 6, 0
	s_sub_i32 s100, s100, s101
	s_cmp_gt_u32 s100, 3
	s_cselect_b32 s101, 0x14000, 0
	s_lshl_b32 s100, s100, 13
	s_add_i32 s100, s100, s101
	s_add_i32 s101, s100, s29
	s_mov_b32 m0, s101
	s_add_i32 s100, s100, s33
	global_load_lds_dwordx4 v[172:173], off
	s_mov_b32 m0, s100
	s_nop 0
	global_load_lds_dwordx4 v[152:153], off
	s_nop 1
	s_branch .Lmo_go

; __device__ __forceinline__ unsigned cvtpk(float lo, float hi) { f32x2_t v = {lo, hi}; bf16x2_t b = __builtin_convertvector(v, bf16x2_t); return __builtin_bit_cast(unsigned, b); }
; template <class BIAS>
; __device__ __forceinline__ void attn_tiles(char* shm, const UnitIO& io, int t_begin, int t_end, const BIAS& B, int tid) {
;     ...
;             float s0 = 0.f;
; #pragma unroll
;             for (int r = 0; r < 16; ++r) c0[r] = __builtin_amdgcn_exp2f(c0[r]);
;             { f32x2_t s2 = (f32x2_t){c0[0], c0[1]};
; #pragma unroll
;               for (int i = 1; i < 8; ++i) s2 += (f32x2_t){c0[2 * i], c0[2 * i + 1]};
;               s0 = s2[0] + s2[1]; }
;             l_reg += s0;
; #pragma unroll
;             for (int i = 0; i < 4; ++i) { pw[0][i] = cvtpk(c0[2 * i], c0[2 * i + 1]); pw[1][i] = cvtpk(c0[8 + 2 * i], c0[9 + 2 * i]); }
;             c1x = c1;
;         }
;         if (act) {
;             const lds_cptr vp = vp0 + sl_c;
;             s16x4 vlo[8], vhi[8];
; #pragma unroll
;             for (int i = 0; i < 8; ++i) { vlo[i] = vtr(vp + (i >> 2) * 4096 + (i & 3) * 1024); vhi[i] = vtr(vp + (i >> 2) * 4096 + (i & 3) * 1024 + 512); }
;             ATT_SBAR();
;             { float s1 = 0.f;
; #pragma unroll
;               for (int r = 0; r < 16; ++r) c1x[r] = __builtin_amdgcn_exp2f(c1x[r]);
;               { f32x2_t s2 = (f32x2_t){c1x[0], c1x[1]};
; #pragma unroll
;                 for (int i = 1; i < 8; ++i) s2 += (f32x2_t){c1x[2 * i], c1x[2 * i + 1]};
;                 s1 = s2[0] + s2[1]; }
;               l_reg += s1;
; #pragma unroll
;               for (int i = 0; i < 4; ++i) { pw[2][i] = cvtpk(c1x[2 * i], c1x[2 * i + 1]); pw[3][i] = cvtpk(c1x[8 + 2 * i], c1x[9 + 2 * i]); } }
;             ATT_SBAR();
;             asm volatile("" : "+v"(vlo[0]), "+v"(vhi[0]), "+v"(vlo[1]), "+v"(vhi[1]), "+v"(vlo[2]), "+v"(vhi[2]), "+v"(vlo[3]), "+v"(vhi[3]));
; #pragma unroll
;             for (int ks = 0; ks < 4; ++ks) { const bf16x8 vf = (bf16x8){vlo[ks][0], vlo[ks][1], vlo[ks][2], vlo[ks][3], vhi[ks][0], vhi[ks][1], vhi[ks][2], vhi[ks][3]};
;                 o[0] = __builtin_amdgcn_mfma_f32_32x32x16_bf16(__builtin_bit_cast(bf16x8, pw[ks]), vf, o[0], 0, 0, 0); }
;             ATT_SBAR();
;             asm volatile("" : "+v"(vlo[4]), "+v"(vhi[4]), "+v"(vlo[5]), "+v"(vhi[5]), "+v"(vlo[6]), "+v"(vhi[6]), "+v"(vlo[7]), "+v"(vhi[7]));
; #pragma unroll
.Lmo_go:
	v_exp_f32_e32 v50, v50
	v_exp_f32_e32 v51, v51
	v_exp_f32_e32 v52, v52
	v_exp_f32_e32 v53, v53
	v_mfma_f32_32x32x16_bf16 v[34:49], v[90:93], v[70:73], v[34:49]
	v_exp_f32_e32 v98, v54
	v_exp_f32_e32 v99, v55
	v_exp_f32_e32 v100, v56
	v_exp_f32_e32 v101, v57
	v_mfma_f32_32x32x16_bf16 v[34:49], v[86:89], v[74:77], v[34:49]
	v_exp_f32_e32 v54, v58
	v_exp_f32_e32 v55, v59
	v_exp_f32_e32 v56, v60
	v_exp_f32_e32 v57, v61
	v_mfma_f32_32x32x16_bf16 v[34:49], v[82:85], v[78:81], v[34:49]
	v_exp_f32_e32 v58, v62
	v_exp_f32_e32 v59, v63
	v_add_f32_e32 v62, v50, v52
	v_add_f32_e32 v63, v51, v53
	v_add_f32_e64 v62, v98, v62
	v_add_f32_e64 v63, v99, v63
	v_exp_f32_e32 v60, v64
	v_exp_f32_e32 v61, v65
	v_add_f32_e32 v62, v100, v62
	v_add_f32_e32 v63, v101, v63
	v_cvt_pk_bf16_f32 v50, v50, v51
	v_add_f32_e32 v62, v54, v62
	v_add_f32_e32 v63, v55, v63
	v_cvt_pk_bf16_f32 v54, v54, v55
	v_add_f32_e32 v62, v56, v62
	v_add_f32_e32 v63, v57, v63
	v_cvt_pk_bf16_f32 v51, v52, v53
	v_add_f32_e32 v62, v58, v62
	v_add_f32_e32 v63, v59, v63
	v_cvt_pk_bf16_f32 v55, v56, v57
	v_add_f32_e32 v62, v60, v62
	v_add_f32_e32 v63, v61, v63
	v_cvt_pk_bf16_f32 v52, v98, v99
	v_add_f32_e32 v62, v62, v63
	v_cvt_pk_bf16_f32 v56, v58, v59
	v_cvt_pk_bf16_f32 v53, v100, v101
	v_cvt_pk_bf16_f32 v57, v60, v61
	v_add_f32_e32 v139, v139, v62
	s_branch .LBB0_311
.Lmo_inact:
	s_and_b64 vcc, exec, s[12:13]
	s_cbranch_vccnz .Lmo_nodmaB
	s_add_i32 s100, s22, 4
	s_cmp_gt_u32 s100, 5
	s_cselect_b32 s101, 6, 0
	s_sub_i32 s100, s100, s101
	s_cmp_gt_u32 s100, 3
	s_cselect_b32 s101, 0x14000, 0
	s_lshl_b32 s100, s100, 13
	s_add_i32 s100, s100, s101
	s_add_i32 s101, s100, s29
	s_mov_b32 m0, s101
	s_add_i32 s100, s100, s33
	global_load_lds_dwordx4 v[172:173], off
	s_mov_b32 m0, s100
	s_nop 0
	global_load_lds_dwordx4 v[152:153], off
.Lmo_nodmaB:
	s_branch .Lmo_endstep
.LBB0_311:
	v_add_u32_e32 v104, s23, v180
	ds_read_b64_tr_b16 v[58:59], v104 offset:32768
	ds_read_b64_tr_b16 v[60:61], v104 offset:33280
	ds_read_b64_tr_b16 v[62:63], v104 offset:33792
	ds_read_b64_tr_b16 v[64:65], v104 offset:34304
	ds_read_b64_tr_b16 v[82:83], v104 offset:34816
	ds_read_b64_tr_b16 v[84:85], v104 offset:35328
	ds_read_b64_tr_b16 v[86:87], v104 offset:35840
	ds_read_b64_tr_b16 v[88:89], v104 offset:36352
	ds_read_b64_tr_b16 v[90:91], v104 offset:36864
	ds_read_b64_tr_b16 v[92:93], v104 offset:37376
	ds_read_b64_tr_b16 v[94:95], v104 offset:37888
	ds_read_b64_tr_b16 v[96:97], v104 offset:38400
	ds_read_b64_tr_b16 v[98:99], v104 offset:38912
	ds_read_b64_tr_b16 v[100:101], v104 offset:39424
	ds_read_b64_tr_b16 v[102:103], v104 offset:39936
	ds_read_b64_tr_b16 v[104:105], v104 offset:40448
	v_exp_f32_e32 v34, v34
	v_exp_f32_e32 v35, v35
	v_exp_f32_e32 v36, v36
	v_exp_f32_e32 v37, v37
	s_waitcnt lgkmcnt(14)
	v_mfma_f32_32x32x16_bf16 v[2:17], v[50:53], v[58:61], v[2:17]
	v_exp_f32_e32 v38, v38
	v_exp_f32_e32 v39, v39
	v_exp_f32_e32 v40, v40
	v_exp_f32_e32 v41, v41
	s_waitcnt lgkmcnt(12)
	v_mfma_f32_32x32x16_bf16 v[2:17], v[54:57], v[62:65], v[2:17]
	v_exp_f32_e32 v42, v42
	v_exp_f32_e32 v43, v43
	v_exp_f32_e32 v44, v44
	v_exp_f32_e32 v45, v45
	s_waitcnt lgkmcnt(6)
	v_mfma_f32_32x32x16_bf16 v[18:33], v[50:53], v[90:93], v[18:33]
	v_add_f32_e32 v106, v36, v34
	v_add_f32_e32 v107, v37, v35
	v_exp_f32_e32 v46, v46
	v_exp_f32_e32 v47, v47
	s_waitcnt lgkmcnt(4)
	v_mfma_f32_32x32x16_bf16 v[18:33], v[54:57], v[94:97], v[18:33]
	v_add_f32_e32 v106, v38, v106
	v_add_f32_e32 v107, v39, v107
	v_exp_f32_e32 v48, v48
	v_exp_f32_e32 v49, v49
	v_add_f32_e32 v106, v40, v106
	v_add_f32_e32 v107, v41, v107
	v_cvt_pk_bf16_f32 v110, v42, v43
	v_add_f32_e32 v106, v42, v106
	v_add_f32_e32 v107, v43, v107
	v_cvt_pk_bf16_f32 v111, v44, v45
	v_add_f32_e32 v106, v44, v106
	v_add_f32_e32 v107, v45, v107
	v_cvt_pk_bf16_f32 v108, v38, v39
	v_add_f32_e32 v106, v46, v106
	v_add_f32_e32 v107, v47, v107
	v_cvt_pk_bf16_f32 v112, v46, v47
	v_add_f32_e32 v106, v48, v106
	v_add_f32_e32 v107, v49, v107
	v_cvt_pk_bf16_f32 v109, v40, v41
	v_add_f32_e32 v117, v106, v107
	v_cvt_pk_bf16_f32 v106, v34, v35
	v_cvt_pk_bf16_f32 v107, v36, v37
	v_cvt_pk_bf16_f32 v113, v48, v49
	s_waitcnt lgkmcnt(0)
	s_nop 0
	v_mfma_f32_32x32x16_bf16 v[2:17], v[106:109], v[82:85], v[2:17]
	v_mfma_f32_32x32x16_bf16 v[2:17], v[110:113], v[86:89], v[2:17]
	v_add_f32_e32 v139, v139, v117
	v_mfma_f32_32x32x16_bf16 v[18:33], v[106:109], v[98:101], v[18:33]
	v_mfma_f32_32x32x16_bf16 v[18:33], v[110:113], v[102:105], v[18:33]
.Lmo_endstep:
	s_bitcmp1_b32 s17, 0
	s_cbranch_scc0 .LBB0_295
	s_cmp_gt_u32 s28, 4
	s_cbranch_scc1 .Lmo_w4
	s_waitcnt vmcnt(0) lgkmcnt(0)
	s_barrier
	s_branch .LBB0_295
